# PEER U token start: next activation row loaded straight into its home registers behind a counted wait (vmcnt(16), or vmcnt(0) when no row prefetch was issued) instead of a full drain + copy per token
# baseline (speedup 1.0000x reference)
.LBB0_1737:
	s_cmp_lg_u32 s48, s56
	s_cbranch_scc1 .LBB0_1741
	s_cmp_gt_i32 s59, 15
	s_cbranch_scc1 .Lunx_drain
	s_waitcnt vmcnt(16)
	s_branch .Lunx_go

.Lunx_go:
	v_mov_b32_e32 v148, v68
	v_mov_b32_e32 v149, v69
	v_mov_b32_e32 v146, v70
	v_mov_b32_e32 v147, v71
	s_cmp_eq_u32 s58, 15
	s_cbranch_scc1 .LBB0_1741
	s_ashr_i32 s30, s58, 31
	s_add_u32 s46, s0, s58
	s_addc_u32 s47, s1, s30
	s_lshl_b64 s[46:47], s[46:47], 10
	v_lshl_add_u64 v[136:137], v[144:145], 0, s[46:47]
	global_load_dwordx4 v[68:71], v[136:137], off offset:1024
